# speedup vs baseline: 1.0256x; 1.0022x over previous
.LBB1_94:
	s_or_b64 exec, exec, s[6:7]
	s_lshl_b32 s4, s28, 1
	s_add_u32 s6, s14, s4
	s_addc_u32 s7, s15, 0
	s_lshl_b64 s[4:5], s[36:37], 1
	s_add_u32 s4, s6, s4
	s_addc_u32 s5, s7, s5
	s_add_u32 s6, s38, s30
	s_addc_u32 s7, s39, 0
	s_lshl_b64 s[6:7], s[6:7], 7
	s_add_u32 s6, s16, s6
	s_addc_u32 s7, s17, s7
	s_waitcnt vmcnt(0)
	v_lshlrev_b32_e32 v6, 3, v13
	v_mov_b32_e32 v7, 0
	v_lshl_add_u64 v[14:15], s[6:7], 0, v[6:7]
	v_lshlrev_b32_e32 v6, 3, v11
	s_waitcnt lgkmcnt(0)
	v_lshl_add_u64 v[20:21], v[14:15], 0, v[6:7]
	global_load_dwordx2 v[24:25], v[20:21], off sc1
	global_load_dwordx2 v[26:27], v[20:21], off offset:8 sc1
	v_lshlrev_b32_e32 v6, 3, v9
	v_lshl_add_u64 v[54:55], v[14:15], 0, v[6:7]
	global_load_dwordx2 v[42:43], v[54:55], off sc1
	global_load_dwordx2 v[44:45], v[54:55], off offset:8 sc1
	v_lshlrev_b32_e32 v6, 3, v5
	v_lshl_add_u64 v[54:55], v[14:15], 0, v[6:7]
	global_load_dwordx2 v[46:47], v[54:55], off sc1
	global_load_dwordx2 v[48:49], v[54:55], off offset:8 sc1
	v_lshlrev_b32_e32 v6, 3, v3
	v_lshl_add_u64 v[54:55], v[14:15], 0, v[6:7]
	global_load_dwordx2 v[50:51], v[54:55], off sc1
	global_load_dwordx2 v[52:53], v[54:55], off offset:8 sc1
	s_nop 0
	s_nop 0
	s_nop 0
	s_nop 0
	s_nop 0
	s_nop 0
	s_nop 0
	s_nop 0
	s_nop 0
	s_nop 0
	s_nop 0
	v_lshl_add_u32 v6, v1, 2, s64
	ds_read_b128 v[20:23], v19
	v_add_u32_e32 v40, 0xc000, v6
	ds_read2_b32 v[28:29], v40 offset1:32
	v_lshlrev_b32_e32 v6, 3, v9
	v_lshl_add_u64 v[30:31], v[14:15], 0, v[6:7]
	s_waitcnt lgkmcnt(1)
	v_cvt_f32_f16_e32 v32, v20
	v_cvt_f32_f16_sdwa v33, v20 dst_sel:DWORD dst_unused:UNUSED_PAD src0_sel:WORD_1
	v_cvt_f32_f16_e32 v20, v21
	v_cvt_f32_f16_sdwa v21, v21 dst_sel:DWORD dst_unused:UNUSED_PAD src0_sel:WORD_1
	v_cvt_f32_f16_e32 v34, v22
	v_cvt_f32_f16_sdwa v35, v22 dst_sel:DWORD dst_unused:UNUSED_PAD src0_sel:WORD_1
	v_cvt_f32_f16_e32 v22, v23
	v_cvt_f32_f16_sdwa v23, v23 dst_sel:DWORD dst_unused:UNUSED_PAD src0_sel:WORD_1
	s_waitcnt lgkmcnt(0)
	v_mov_b32_e32 v6, v29
	v_mov_b32_e32 v11, v7
	v_mov_b32_e32 v13, v7
	v_lshl_add_u64 v[10:11], s[4:5], 0, v[10:11]
	v_lshl_add_u64 v[12:13], v[10:11], 0, v[12:13]
	v_mov_b32_e32 v9, v7
	v_lshl_add_u64 v[8:9], v[10:11], 0, v[8:9]
	s_waitcnt vmcnt(7)
	v_cvt_f32_f16_e32 v36, v24
	v_cvt_f32_f16_sdwa v37, v24 dst_sel:DWORD dst_unused:UNUSED_PAD src0_sel:WORD_1
	v_cvt_f32_f16_e32 v24, v25
	v_cvt_f32_f16_sdwa v25, v25 dst_sel:DWORD dst_unused:UNUSED_PAD src0_sel:WORD_1
	s_waitcnt vmcnt(6)
	v_cvt_f32_f16_e32 v38, v26
	v_cvt_f32_f16_sdwa v39, v26 dst_sel:DWORD dst_unused:UNUSED_PAD src0_sel:WORD_1
	v_cvt_f32_f16_e32 v26, v27
	v_cvt_f32_f16_sdwa v27, v27 dst_sel:DWORD dst_unused:UNUSED_PAD src0_sel:WORD_1
	v_pk_mul_f32 v[36:37], v[6:7], v[36:37] op_sel_hi:[0,1]
	v_pk_mul_f32 v[24:25], v[6:7], v[24:25] op_sel_hi:[0,1]
	v_pk_mul_f32 v[38:39], v[6:7], v[38:39] op_sel_hi:[0,1]
	v_pk_mul_f32 v[26:27], v[6:7], v[26:27] op_sel_hi:[0,1]
	v_pk_fma_f32 v[32:33], v[28:29], v[32:33], v[36:37] op_sel_hi:[0,1,1]
	v_pk_fma_f32 v[24:25], v[28:29], v[20:21], v[24:25] op_sel_hi:[0,1,1]
	v_pk_fma_f32 v[34:35], v[28:29], v[34:35], v[38:39] op_sel_hi:[0,1,1]
	v_pk_fma_f32 v[26:27], v[28:29], v[22:23], v[26:27] op_sel_hi:[0,1,1]
	v_cvt_pk_f16_f32 v20, v32, v33
	v_cvt_pk_f16_f32 v21, v24, v25
	v_cvt_pk_f16_f32 v22, v34, v35
	v_cvt_pk_f16_f32 v23, v26, v27
	global_store_dwordx4 v[12:13], v[20:23], off sc1
	s_waitcnt vmcnt(5)
	v_mov_b32_e32 v12, v42
	v_mov_b32_e32 v13, v43
	v_mov_b32_e32 v22, v44
	v_mov_b32_e32 v23, v45
	ds_read_b128 v[18:21], v18
	ds_read2_b32 v[24:25], v40 offset0:8 offset1:40
	v_lshlrev_b32_e32 v6, 3, v5
	v_lshl_add_u64 v[26:27], v[14:15], 0, v[6:7]
	v_mov_b32_e32 v5, v7
	s_waitcnt lgkmcnt(1)
	v_cvt_f32_f16_e32 v28, v18
	v_cvt_f32_f16_sdwa v29, v18 dst_sel:DWORD dst_unused:UNUSED_PAD src0_sel:WORD_1
	v_cvt_f32_f16_e32 v18, v19
	v_cvt_f32_f16_sdwa v19, v19 dst_sel:DWORD dst_unused:UNUSED_PAD src0_sel:WORD_1
	v_cvt_f32_f16_e32 v30, v20
	v_cvt_f32_f16_sdwa v31, v20 dst_sel:DWORD dst_unused:UNUSED_PAD src0_sel:WORD_1
	v_cvt_f32_f16_e32 v20, v21
	v_cvt_f32_f16_sdwa v21, v21 dst_sel:DWORD dst_unused:UNUSED_PAD src0_sel:WORD_1
	s_waitcnt lgkmcnt(0)
	v_mov_b32_e32 v6, v25
	v_lshl_add_u64 v[4:5], v[10:11], 0, v[4:5]
	s_waitcnt vmcnt(5)
	v_cvt_f32_f16_e32 v32, v12
	v_cvt_f32_f16_sdwa v33, v12 dst_sel:DWORD dst_unused:UNUSED_PAD src0_sel:WORD_1
	v_cvt_f32_f16_e32 v12, v13
	v_cvt_f32_f16_sdwa v13, v13 dst_sel:DWORD dst_unused:UNUSED_PAD src0_sel:WORD_1
	s_waitcnt vmcnt(5)
	v_cvt_f32_f16_e32 v34, v22
	v_cvt_f32_f16_sdwa v35, v22 dst_sel:DWORD dst_unused:UNUSED_PAD src0_sel:WORD_1
	v_cvt_f32_f16_e32 v22, v23
	v_cvt_f32_f16_sdwa v23, v23 dst_sel:DWORD dst_unused:UNUSED_PAD src0_sel:WORD_1
	v_pk_mul_f32 v[32:33], v[6:7], v[32:33] op_sel_hi:[0,1]
	v_pk_mul_f32 v[12:13], v[6:7], v[12:13] op_sel_hi:[0,1]
	v_pk_mul_f32 v[34:35], v[6:7], v[34:35] op_sel_hi:[0,1]
	v_pk_mul_f32 v[22:23], v[6:7], v[22:23] op_sel_hi:[0,1]
	v_pk_fma_f32 v[28:29], v[24:25], v[28:29], v[32:33] op_sel_hi:[0,1,1]
	v_pk_fma_f32 v[12:13], v[24:25], v[18:19], v[12:13] op_sel_hi:[0,1,1]
	v_pk_fma_f32 v[30:31], v[24:25], v[30:31], v[34:35] op_sel_hi:[0,1,1]
	v_pk_fma_f32 v[22:23], v[24:25], v[20:21], v[22:23] op_sel_hi:[0,1,1]
	v_cvt_pk_f16_f32 v18, v28, v29
	v_cvt_pk_f16_f32 v19, v12, v13
	v_cvt_pk_f16_f32 v20, v30, v31
	v_cvt_pk_f16_f32 v21, v22, v23
	global_store_dwordx4 v[8:9], v[18:21], off sc1
	s_waitcnt vmcnt(4)
	v_mov_b32_e32 v8, v46
	v_mov_b32_e32 v9, v47
	v_mov_b32_e32 v12, v48
	v_mov_b32_e32 v13, v49
	ds_read_b128 v[18:21], v17
	ds_read2_b32 v[22:23], v40 offset0:16 offset1:48
	v_lshlrev_b32_e32 v6, 3, v3
	v_lshl_add_u64 v[24:25], v[14:15], 0, v[6:7]
	v_mov_b32_e32 v3, v7
	s_waitcnt lgkmcnt(1)
	v_cvt_f32_f16_e32 v14, v18
	v_cvt_f32_f16_sdwa v15, v18 dst_sel:DWORD dst_unused:UNUSED_PAD src0_sel:WORD_1
	v_cvt_f32_f16_e32 v18, v19
	v_cvt_f32_f16_sdwa v19, v19 dst_sel:DWORD dst_unused:UNUSED_PAD src0_sel:WORD_1
	v_cvt_f32_f16_e32 v26, v20
	v_cvt_f32_f16_sdwa v27, v20 dst_sel:DWORD dst_unused:UNUSED_PAD src0_sel:WORD_1
	v_cvt_f32_f16_e32 v20, v21
	v_cvt_f32_f16_sdwa v21, v21 dst_sel:DWORD dst_unused:UNUSED_PAD src0_sel:WORD_1
	s_waitcnt lgkmcnt(0)
	v_mov_b32_e32 v6, v23
	v_lshl_add_u64 v[2:3], v[10:11], 0, v[2:3]
	s_waitcnt vmcnt(4)
	v_cvt_f32_f16_e32 v28, v8
	v_cvt_f32_f16_sdwa v29, v8 dst_sel:DWORD dst_unused:UNUSED_PAD src0_sel:WORD_1
	v_cvt_f32_f16_e32 v8, v9
	v_cvt_f32_f16_sdwa v9, v9 dst_sel:DWORD dst_unused:UNUSED_PAD src0_sel:WORD_1
	s_waitcnt vmcnt(4)
	v_cvt_f32_f16_e32 v30, v12
	v_cvt_f32_f16_sdwa v31, v12 dst_sel:DWORD dst_unused:UNUSED_PAD src0_sel:WORD_1
	v_cvt_f32_f16_e32 v12, v13
	v_cvt_f32_f16_sdwa v13, v13 dst_sel:DWORD dst_unused:UNUSED_PAD src0_sel:WORD_1
	v_pk_mul_f32 v[28:29], v[6:7], v[28:29] op_sel_hi:[0,1]
	v_pk_mul_f32 v[8:9], v[6:7], v[8:9] op_sel_hi:[0,1]
	v_pk_mul_f32 v[30:31], v[6:7], v[30:31] op_sel_hi:[0,1]
	v_pk_mul_f32 v[12:13], v[6:7], v[12:13] op_sel_hi:[0,1]
	v_pk_fma_f32 v[14:15], v[22:23], v[14:15], v[28:29] op_sel_hi:[0,1,1]
	v_pk_fma_f32 v[8:9], v[22:23], v[18:19], v[8:9] op_sel_hi:[0,1,1]
	v_pk_fma_f32 v[18:19], v[22:23], v[26:27], v[30:31] op_sel_hi:[0,1,1]
	v_pk_fma_f32 v[20:21], v[22:23], v[20:21], v[12:13] op_sel_hi:[0,1,1]
	v_cvt_pk_f16_f32 v12, v14, v15
	v_cvt_pk_f16_f32 v13, v8, v9
	v_cvt_pk_f16_f32 v14, v18, v19
	v_cvt_pk_f16_f32 v15, v20, v21
	global_store_dwordx4 v[4:5], v[12:15], off sc1
	s_waitcnt vmcnt(3)
	v_mov_b32_e32 v4, v50
	v_mov_b32_e32 v5, v51
	v_mov_b32_e32 v8, v52
	v_mov_b32_e32 v9, v53
	ds_read_b128 v[12:15], v16
	ds_read2_b32 v[16:17], v40 offset0:24 offset1:56
	s_waitcnt lgkmcnt(1)
	v_cvt_f32_f16_e32 v6, v12
	v_cvt_f32_f16_sdwa v7, v12 dst_sel:DWORD dst_unused:UNUSED_PAD src0_sel:WORD_1
	v_cvt_f32_f16_e32 v18, v13
	v_cvt_f32_f16_sdwa v19, v13 dst_sel:DWORD dst_unused:UNUSED_PAD src0_sel:WORD_1
	v_cvt_f32_f16_e32 v20, v14
	v_cvt_f32_f16_sdwa v21, v14 dst_sel:DWORD dst_unused:UNUSED_PAD src0_sel:WORD_1
	v_cvt_f32_f16_e32 v14, v15
	v_cvt_f32_f16_sdwa v15, v15 dst_sel:DWORD dst_unused:UNUSED_PAD src0_sel:WORD_1
	s_waitcnt lgkmcnt(0)
	v_mov_b32_e32 v12, v17
	s_waitcnt vmcnt(3)
	v_cvt_f32_f16_e32 v22, v4
	v_cvt_f32_f16_sdwa v23, v4 dst_sel:DWORD dst_unused:UNUSED_PAD src0_sel:WORD_1
	v_cvt_f32_f16_e32 v4, v5
	v_cvt_f32_f16_sdwa v5, v5 dst_sel:DWORD dst_unused:UNUSED_PAD src0_sel:WORD_1
	s_waitcnt vmcnt(3)
	v_cvt_f32_f16_e32 v24, v8
	v_cvt_f32_f16_sdwa v25, v8 dst_sel:DWORD dst_unused:UNUSED_PAD src0_sel:WORD_1
	v_cvt_f32_f16_e32 v8, v9
	v_cvt_f32_f16_sdwa v9, v9 dst_sel:DWORD dst_unused:UNUSED_PAD src0_sel:WORD_1
	v_pk_mul_f32 v[22:23], v[12:13], v[22:23] op_sel_hi:[0,1]
	v_pk_mul_f32 v[4:5], v[12:13], v[4:5] op_sel_hi:[0,1]
	v_pk_mul_f32 v[24:25], v[12:13], v[24:25] op_sel_hi:[0,1]
	v_pk_mul_f32 v[8:9], v[12:13], v[8:9] op_sel_hi:[0,1]
	v_pk_fma_f32 v[6:7], v[16:17], v[6:7], v[22:23] op_sel_hi:[0,1,1]
	v_pk_fma_f32 v[12:13], v[16:17], v[18:19], v[4:5] op_sel_hi:[0,1,1]
	v_pk_fma_f32 v[18:19], v[16:17], v[20:21], v[24:25] op_sel_hi:[0,1,1]
	v_pk_fma_f32 v[8:9], v[16:17], v[14:15], v[8:9] op_sel_hi:[0,1,1]
	v_cvt_pk_f16_f32 v4, v6, v7
	v_cvt_pk_f16_f32 v5, v12, v13
	v_cvt_pk_f16_f32 v6, v18, v19
	v_cvt_pk_f16_f32 v7, v8, v9
	global_store_dwordx4 v[2:3], v[4:7], off sc1

.LBB1_220:
	s_or_b64 exec, exec, s[18:19]
	s_lshl_b32 s0, s50, 1
	s_add_u32 s7, s14, s0
	s_addc_u32 s18, s15, 0
	s_lshl_b64 s[0:1], s[24:25], 1
	s_add_u32 s0, s7, s0
	s_addc_u32 s1, s18, s1
	s_add_u32 s6, s20, s6
	s_addc_u32 s7, s21, 0
	s_lshl_b64 s[6:7], s[6:7], 7
	s_add_u32 s6, s16, s6
	s_addc_u32 s7, s17, s7
	s_waitcnt vmcnt(0)
	v_lshlrev_b32_e32 v6, 3, v13
	v_mov_b32_e32 v7, 0
	v_lshl_add_u64 v[14:15], s[6:7], 0, v[6:7]
	v_lshlrev_b32_e32 v6, 3, v11
	s_waitcnt lgkmcnt(0)
	v_lshl_add_u64 v[20:21], v[14:15], 0, v[6:7]
	global_load_dwordx2 v[24:25], v[20:21], off sc1
	global_load_dwordx2 v[26:27], v[20:21], off offset:8 sc1
	v_lshlrev_b32_e32 v6, 3, v9
	v_lshl_add_u64 v[54:55], v[14:15], 0, v[6:7]
	global_load_dwordx2 v[42:43], v[54:55], off sc1
	global_load_dwordx2 v[44:45], v[54:55], off offset:8 sc1
	v_lshlrev_b32_e32 v6, 3, v5
	v_lshl_add_u64 v[54:55], v[14:15], 0, v[6:7]
	global_load_dwordx2 v[46:47], v[54:55], off sc1
	global_load_dwordx2 v[48:49], v[54:55], off offset:8 sc1
	v_lshlrev_b32_e32 v6, 3, v3
	v_lshl_add_u64 v[54:55], v[14:15], 0, v[6:7]
	global_load_dwordx2 v[50:51], v[54:55], off sc1
	global_load_dwordx2 v[52:53], v[54:55], off offset:8 sc1
	s_nop 0
	s_nop 0
	s_nop 0
	s_nop 0
	s_nop 0
	s_nop 0
	s_nop 0
	s_nop 0
	s_nop 0
	s_nop 0
	s_nop 0
	v_lshl_add_u32 v6, v199, 2, s51
	ds_read_b128 v[20:23], v19
	v_add_u32_e32 v40, 0xc000, v6
	ds_read2_b32 v[28:29], v40 offset1:32
	v_lshlrev_b32_e32 v6, 3, v9
	v_lshl_add_u64 v[30:31], v[14:15], 0, v[6:7]
	s_waitcnt lgkmcnt(1)
	v_cvt_f32_f16_e32 v32, v20
	v_cvt_f32_f16_sdwa v33, v20 dst_sel:DWORD dst_unused:UNUSED_PAD src0_sel:WORD_1
	v_cvt_f32_f16_e32 v20, v21
	v_cvt_f32_f16_sdwa v21, v21 dst_sel:DWORD dst_unused:UNUSED_PAD src0_sel:WORD_1
	v_cvt_f32_f16_e32 v34, v22
	v_cvt_f32_f16_sdwa v35, v22 dst_sel:DWORD dst_unused:UNUSED_PAD src0_sel:WORD_1
	v_cvt_f32_f16_e32 v22, v23
	v_cvt_f32_f16_sdwa v23, v23 dst_sel:DWORD dst_unused:UNUSED_PAD src0_sel:WORD_1
	s_waitcnt lgkmcnt(0)
	v_mov_b32_e32 v6, v29
	v_mov_b32_e32 v11, v7
	v_mov_b32_e32 v13, v7
	v_lshl_add_u64 v[10:11], s[0:1], 0, v[10:11]
	v_lshl_add_u64 v[12:13], v[10:11], 0, v[12:13]
	v_mov_b32_e32 v9, v7
	v_lshl_add_u64 v[8:9], v[10:11], 0, v[8:9]
	s_waitcnt vmcnt(7)
	v_cvt_f32_f16_e32 v36, v24
	v_cvt_f32_f16_sdwa v37, v24 dst_sel:DWORD dst_unused:UNUSED_PAD src0_sel:WORD_1
	v_cvt_f32_f16_e32 v24, v25
	v_cvt_f32_f16_sdwa v25, v25 dst_sel:DWORD dst_unused:UNUSED_PAD src0_sel:WORD_1
	s_waitcnt vmcnt(6)
	v_cvt_f32_f16_e32 v38, v26
	v_cvt_f32_f16_sdwa v39, v26 dst_sel:DWORD dst_unused:UNUSED_PAD src0_sel:WORD_1
	v_cvt_f32_f16_e32 v26, v27
	v_cvt_f32_f16_sdwa v27, v27 dst_sel:DWORD dst_unused:UNUSED_PAD src0_sel:WORD_1
	v_pk_mul_f32 v[36:37], v[6:7], v[36:37] op_sel_hi:[0,1]
	v_pk_mul_f32 v[24:25], v[6:7], v[24:25] op_sel_hi:[0,1]
	v_pk_mul_f32 v[38:39], v[6:7], v[38:39] op_sel_hi:[0,1]
	v_pk_mul_f32 v[26:27], v[6:7], v[26:27] op_sel_hi:[0,1]
	v_pk_fma_f32 v[32:33], v[28:29], v[32:33], v[36:37] op_sel_hi:[0,1,1]
	v_pk_fma_f32 v[24:25], v[28:29], v[20:21], v[24:25] op_sel_hi:[0,1,1]
	v_pk_fma_f32 v[34:35], v[28:29], v[34:35], v[38:39] op_sel_hi:[0,1,1]
	v_pk_fma_f32 v[26:27], v[28:29], v[22:23], v[26:27] op_sel_hi:[0,1,1]
	v_cvt_pk_f16_f32 v20, v32, v33
	v_cvt_pk_f16_f32 v21, v24, v25
	v_cvt_pk_f16_f32 v22, v34, v35
	v_cvt_pk_f16_f32 v23, v26, v27
	global_store_dwordx4 v[12:13], v[20:23], off sc1
	s_waitcnt vmcnt(5)
	v_mov_b32_e32 v12, v42
	v_mov_b32_e32 v13, v43
	v_mov_b32_e32 v22, v44
	v_mov_b32_e32 v23, v45
	ds_read_b128 v[18:21], v18
	ds_read2_b32 v[24:25], v40 offset0:8 offset1:40
	v_lshlrev_b32_e32 v6, 3, v5
	v_lshl_add_u64 v[26:27], v[14:15], 0, v[6:7]
	v_mov_b32_e32 v5, v7
	s_waitcnt lgkmcnt(1)
	v_cvt_f32_f16_e32 v28, v18
	v_cvt_f32_f16_sdwa v29, v18 dst_sel:DWORD dst_unused:UNUSED_PAD src0_sel:WORD_1
	v_cvt_f32_f16_e32 v18, v19
	v_cvt_f32_f16_sdwa v19, v19 dst_sel:DWORD dst_unused:UNUSED_PAD src0_sel:WORD_1
	v_cvt_f32_f16_e32 v30, v20
	v_cvt_f32_f16_sdwa v31, v20 dst_sel:DWORD dst_unused:UNUSED_PAD src0_sel:WORD_1
	v_cvt_f32_f16_e32 v20, v21
	v_cvt_f32_f16_sdwa v21, v21 dst_sel:DWORD dst_unused:UNUSED_PAD src0_sel:WORD_1
	s_waitcnt lgkmcnt(0)
	v_mov_b32_e32 v6, v25
	v_lshl_add_u64 v[4:5], v[10:11], 0, v[4:5]
	s_waitcnt vmcnt(5)
	v_cvt_f32_f16_e32 v32, v12
	v_cvt_f32_f16_sdwa v33, v12 dst_sel:DWORD dst_unused:UNUSED_PAD src0_sel:WORD_1
	v_cvt_f32_f16_e32 v12, v13
	v_cvt_f32_f16_sdwa v13, v13 dst_sel:DWORD dst_unused:UNUSED_PAD src0_sel:WORD_1
	s_waitcnt vmcnt(5)
	v_cvt_f32_f16_e32 v34, v22
	v_cvt_f32_f16_sdwa v35, v22 dst_sel:DWORD dst_unused:UNUSED_PAD src0_sel:WORD_1
	v_cvt_f32_f16_e32 v22, v23
	v_cvt_f32_f16_sdwa v23, v23 dst_sel:DWORD dst_unused:UNUSED_PAD src0_sel:WORD_1
	v_pk_mul_f32 v[32:33], v[6:7], v[32:33] op_sel_hi:[0,1]
	v_pk_mul_f32 v[12:13], v[6:7], v[12:13] op_sel_hi:[0,1]
	v_pk_mul_f32 v[34:35], v[6:7], v[34:35] op_sel_hi:[0,1]
	v_pk_mul_f32 v[22:23], v[6:7], v[22:23] op_sel_hi:[0,1]
	v_pk_fma_f32 v[28:29], v[24:25], v[28:29], v[32:33] op_sel_hi:[0,1,1]
	v_pk_fma_f32 v[12:13], v[24:25], v[18:19], v[12:13] op_sel_hi:[0,1,1]
	v_pk_fma_f32 v[30:31], v[24:25], v[30:31], v[34:35] op_sel_hi:[0,1,1]
	v_pk_fma_f32 v[22:23], v[24:25], v[20:21], v[22:23] op_sel_hi:[0,1,1]
	v_cvt_pk_f16_f32 v18, v28, v29
	v_cvt_pk_f16_f32 v19, v12, v13
	v_cvt_pk_f16_f32 v20, v30, v31
	v_cvt_pk_f16_f32 v21, v22, v23
	global_store_dwordx4 v[8:9], v[18:21], off sc1
	s_waitcnt vmcnt(4)
	v_mov_b32_e32 v8, v46
	v_mov_b32_e32 v9, v47
	v_mov_b32_e32 v12, v48
	v_mov_b32_e32 v13, v49
	ds_read_b128 v[18:21], v17
	ds_read2_b32 v[22:23], v40 offset0:16 offset1:48
	v_lshlrev_b32_e32 v6, 3, v3
	v_lshl_add_u64 v[24:25], v[14:15], 0, v[6:7]
	v_mov_b32_e32 v3, v7
	s_waitcnt lgkmcnt(1)
	v_cvt_f32_f16_e32 v14, v18
	v_cvt_f32_f16_sdwa v15, v18 dst_sel:DWORD dst_unused:UNUSED_PAD src0_sel:WORD_1
	v_cvt_f32_f16_e32 v18, v19
	v_cvt_f32_f16_sdwa v19, v19 dst_sel:DWORD dst_unused:UNUSED_PAD src0_sel:WORD_1
	v_cvt_f32_f16_e32 v26, v20
	v_cvt_f32_f16_sdwa v27, v20 dst_sel:DWORD dst_unused:UNUSED_PAD src0_sel:WORD_1
	v_cvt_f32_f16_e32 v20, v21
	v_cvt_f32_f16_sdwa v21, v21 dst_sel:DWORD dst_unused:UNUSED_PAD src0_sel:WORD_1
	s_waitcnt lgkmcnt(0)
	v_mov_b32_e32 v6, v23
	v_lshl_add_u64 v[2:3], v[10:11], 0, v[2:3]
	s_waitcnt vmcnt(4)
	v_cvt_f32_f16_e32 v28, v8
	v_cvt_f32_f16_sdwa v29, v8 dst_sel:DWORD dst_unused:UNUSED_PAD src0_sel:WORD_1
	v_cvt_f32_f16_e32 v8, v9
	v_cvt_f32_f16_sdwa v9, v9 dst_sel:DWORD dst_unused:UNUSED_PAD src0_sel:WORD_1
	s_waitcnt vmcnt(4)
	v_cvt_f32_f16_e32 v30, v12
	v_cvt_f32_f16_sdwa v31, v12 dst_sel:DWORD dst_unused:UNUSED_PAD src0_sel:WORD_1
	v_cvt_f32_f16_e32 v12, v13
	v_cvt_f32_f16_sdwa v13, v13 dst_sel:DWORD dst_unused:UNUSED_PAD src0_sel:WORD_1
	v_pk_mul_f32 v[28:29], v[6:7], v[28:29] op_sel_hi:[0,1]
	v_pk_mul_f32 v[8:9], v[6:7], v[8:9] op_sel_hi:[0,1]
	v_pk_mul_f32 v[30:31], v[6:7], v[30:31] op_sel_hi:[0,1]
	v_pk_mul_f32 v[12:13], v[6:7], v[12:13] op_sel_hi:[0,1]
	v_pk_fma_f32 v[14:15], v[22:23], v[14:15], v[28:29] op_sel_hi:[0,1,1]
	v_pk_fma_f32 v[8:9], v[22:23], v[18:19], v[8:9] op_sel_hi:[0,1,1]
	v_pk_fma_f32 v[18:19], v[22:23], v[26:27], v[30:31] op_sel_hi:[0,1,1]
	v_pk_fma_f32 v[20:21], v[22:23], v[20:21], v[12:13] op_sel_hi:[0,1,1]
	v_cvt_pk_f16_f32 v12, v14, v15
	v_cvt_pk_f16_f32 v13, v8, v9
	v_cvt_pk_f16_f32 v14, v18, v19
	v_cvt_pk_f16_f32 v15, v20, v21
	global_store_dwordx4 v[4:5], v[12:15], off sc1
	s_waitcnt vmcnt(3)
	v_mov_b32_e32 v4, v50
	v_mov_b32_e32 v5, v51
	v_mov_b32_e32 v8, v52
	v_mov_b32_e32 v9, v53
	ds_read_b128 v[12:15], v16
	ds_read2_b32 v[16:17], v40 offset0:24 offset1:56
	s_waitcnt lgkmcnt(1)
	v_cvt_f32_f16_e32 v6, v12
	v_cvt_f32_f16_sdwa v7, v12 dst_sel:DWORD dst_unused:UNUSED_PAD src0_sel:WORD_1
	v_cvt_f32_f16_e32 v18, v13
	v_cvt_f32_f16_sdwa v19, v13 dst_sel:DWORD dst_unused:UNUSED_PAD src0_sel:WORD_1
	v_cvt_f32_f16_e32 v20, v14
	v_cvt_f32_f16_sdwa v21, v14 dst_sel:DWORD dst_unused:UNUSED_PAD src0_sel:WORD_1
	v_cvt_f32_f16_e32 v14, v15
	v_cvt_f32_f16_sdwa v15, v15 dst_sel:DWORD dst_unused:UNUSED_PAD src0_sel:WORD_1
	s_waitcnt lgkmcnt(0)
	v_mov_b32_e32 v12, v17
	s_waitcnt vmcnt(3)
	v_cvt_f32_f16_e32 v22, v4
	v_cvt_f32_f16_sdwa v23, v4 dst_sel:DWORD dst_unused:UNUSED_PAD src0_sel:WORD_1
	v_cvt_f32_f16_e32 v4, v5
	v_cvt_f32_f16_sdwa v5, v5 dst_sel:DWORD dst_unused:UNUSED_PAD src0_sel:WORD_1
	s_waitcnt vmcnt(3)
	v_cvt_f32_f16_e32 v24, v8
	v_cvt_f32_f16_sdwa v25, v8 dst_sel:DWORD dst_unused:UNUSED_PAD src0_sel:WORD_1
	v_cvt_f32_f16_e32 v8, v9
	v_cvt_f32_f16_sdwa v9, v9 dst_sel:DWORD dst_unused:UNUSED_PAD src0_sel:WORD_1
	v_pk_mul_f32 v[22:23], v[12:13], v[22:23] op_sel_hi:[0,1]
	v_pk_mul_f32 v[4:5], v[12:13], v[4:5] op_sel_hi:[0,1]
	v_pk_mul_f32 v[24:25], v[12:13], v[24:25] op_sel_hi:[0,1]
	v_pk_mul_f32 v[8:9], v[12:13], v[8:9] op_sel_hi:[0,1]
	v_pk_fma_f32 v[6:7], v[16:17], v[6:7], v[22:23] op_sel_hi:[0,1,1]
	v_pk_fma_f32 v[12:13], v[16:17], v[18:19], v[4:5] op_sel_hi:[0,1,1]
	v_pk_fma_f32 v[18:19], v[16:17], v[20:21], v[24:25] op_sel_hi:[0,1,1]
	v_pk_fma_f32 v[8:9], v[16:17], v[14:15], v[8:9] op_sel_hi:[0,1,1]
	v_cvt_pk_f16_f32 v4, v6, v7
	v_cvt_pk_f16_f32 v5, v12, v13
	v_cvt_pk_f16_f32 v6, v18, v19
	v_cvt_pk_f16_f32 v7, v8, v9
	global_store_dwordx4 v[2:3], v[4:7], off sc1
